# v53 + nt pair on x1: P7 epilogue stores and P8 LN2 row loads
# baseline (speedup 1.0000x reference)
.LBB0_1150:
	v_lshl_or_b32 v6, s71, 8, v202
	v_ashrrev_i32_e32 v7, 31, v6
	v_add_u32_e32 v10, s70, v200
	v_lshl_add_u64 v[8:9], v[6:7], 2, s[14:15]
	v_ashrrev_i32_e32 v11, 31, v10
	global_load_dwordx4 v[16:19], v[8:9], off
	global_load_dwordx4 v[20:23], v[8:9], off offset:64
	global_load_dwordx4 v[24:27], v[8:9], off offset:512
	global_load_dwordx4 v[28:31], v[8:9], off offset:576
	v_lshlrev_b64 v[10:11], 11, v[10:11]
	v_lshl_add_u64 v[6:7], v[10:11], 0, v[6:7]
	v_lshlrev_b32_e32 v14, 2, v6
	global_load_dwordx4 v[212:215], v14, s[6:7] nt
	global_load_dwordx4 v[216:219], v14, s[6:7] offset:64 nt
	global_load_dwordx4 v[220:223], v14, s[6:7] offset:512 nt
	global_load_dwordx4 v[224:227], v14, s[6:7] offset:576 nt
	v_add_u32_e32 v12, s24, v14
	global_load_dwordx4 v[228:231], v12, s[6:7] nt
	global_load_dwordx4 v[232:235], v12, s[6:7] offset:64 nt
	global_load_dwordx4 v[236:239], v12, s[6:7] offset:512 nt
	global_load_dwordx4 v[240:243], v12, s[6:7] offset:576 nt
	v_add_u32_e32 v12, s10, v14
	global_load_dwordx4 v[244:247], v12, s[6:7] nt
	global_load_dwordx4 v[248:251], v12, s[6:7] offset:64 nt
	global_load_dwordx4 v[2:5], v12, s[6:7] offset:512 nt
	global_load_dwordx4 v[8:11], v12, s[6:7] offset:576 nt
	s_andn2_b64 vcc, exec, s[0:1]
	s_mov_b64 s[0:1], -1
	s_nop 15
	s_waitcnt vmcnt(12)
	v_pk_mul_f32 v[16:17], v[16:17], s[22:23] op_sel_hi:[1,0]
	v_pk_mul_f32 v[18:19], v[18:19], s[22:23] op_sel_hi:[1,0]
	v_pk_mul_f32 v[20:21], v[20:21], s[22:23] op_sel_hi:[1,0]
	v_pk_mul_f32 v[22:23], v[22:23], s[22:23] op_sel_hi:[1,0]
	v_pk_mul_f32 v[24:25], v[24:25], s[22:23] op_sel_hi:[1,0]
	v_pk_mul_f32 v[26:27], v[26:27], s[22:23] op_sel_hi:[1,0]
	v_pk_mul_f32 v[28:29], v[28:29], s[22:23] op_sel_hi:[1,0]
	v_pk_mul_f32 v[30:31], v[30:31], s[22:23] op_sel_hi:[1,0]
	s_waitcnt vmcnt(8)
	v_pk_fma_f32 v[214:215], v[160:161], v[18:19], v[214:215]
	v_pk_fma_f32 v[212:213], v[158:159], v[16:17], v[212:213]
	v_pk_fma_f32 v[218:219], v[156:157], v[22:23], v[218:219]
	v_pk_fma_f32 v[216:217], v[154:155], v[20:21], v[216:217]
	v_pk_fma_f32 v[222:223], v[152:153], v[26:27], v[222:223]
	v_pk_fma_f32 v[220:221], v[150:151], v[24:25], v[220:221]
	v_pk_fma_f32 v[226:227], v[140:141], v[30:31], v[226:227]
	v_pk_fma_f32 v[224:225], v[138:139], v[28:29], v[224:225]
	global_store_dwordx4 v14, v[212:215], s[48:49] nt
	global_store_dwordx4 v14, v[216:219], s[48:49] offset:64 nt
	global_store_dwordx4 v14, v[220:223], s[48:49] offset:512 nt
	global_store_dwordx4 v14, v[224:227], s[48:49] offset:576 nt
	v_add_u32_e32 v12, s26, v14
	global_load_dwordx4 v[212:215], v12, s[6:7] nt
	global_load_dwordx4 v[216:219], v12, s[6:7] offset:64 nt
	global_load_dwordx4 v[220:223], v12, s[6:7] offset:512 nt
	global_load_dwordx4 v[224:227], v12, s[6:7] offset:576 nt
	s_waitcnt vmcnt(8)
	v_pk_fma_f32 v[230:231], v[148:149], v[18:19], v[230:231]
	v_pk_fma_f32 v[228:229], v[146:147], v[16:17], v[228:229]
	v_pk_fma_f32 v[234:235], v[144:145], v[22:23], v[234:235]
	v_pk_fma_f32 v[232:233], v[142:143], v[20:21], v[232:233]
	v_pk_fma_f32 v[238:239], v[136:137], v[26:27], v[238:239]
	v_pk_fma_f32 v[236:237], v[134:135], v[24:25], v[236:237]
	v_pk_fma_f32 v[242:243], v[124:125], v[30:31], v[242:243]
	v_pk_fma_f32 v[240:241], v[122:123], v[28:29], v[240:241]
	v_add_u32_e32 v13, s24, v14
	global_store_dwordx4 v13, v[228:231], s[48:49] nt
	global_store_dwordx4 v13, v[232:235], s[48:49] offset:64 nt
	global_store_dwordx4 v13, v[236:239], s[48:49] offset:512 nt
	global_store_dwordx4 v13, v[240:243], s[48:49] offset:576 nt
	v_add_u32_e32 v12, s28, v14
	global_load_dwordx4 v[228:231], v12, s[6:7] nt
	global_load_dwordx4 v[232:235], v12, s[6:7] offset:64 nt
	global_load_dwordx4 v[236:239], v12, s[6:7] offset:512 nt
	global_load_dwordx4 v[240:243], v12, s[6:7] offset:576 nt
	s_waitcnt vmcnt(8)
	v_pk_fma_f32 v[246:247], v[132:133], v[18:19], v[246:247]
	v_pk_fma_f32 v[244:245], v[130:131], v[16:17], v[244:245]
	v_pk_fma_f32 v[250:251], v[128:129], v[22:23], v[250:251]
	v_pk_fma_f32 v[248:249], v[126:127], v[20:21], v[248:249]
	v_pk_fma_f32 v[4:5], v[120:121], v[26:27], v[4:5]
	v_pk_fma_f32 v[2:3], v[118:119], v[24:25], v[2:3]
	v_pk_fma_f32 v[10:11], v[108:109], v[30:31], v[10:11]
	v_pk_fma_f32 v[8:9], v[106:107], v[28:29], v[8:9]
	v_add_u32_e32 v13, s10, v14
	global_store_dwordx4 v13, v[244:247], s[48:49] nt
	global_store_dwordx4 v13, v[248:251], s[48:49] offset:64 nt
	global_store_dwordx4 v13, v[2:5], s[48:49] offset:512 nt
	global_store_dwordx4 v13, v[8:11], s[48:49] offset:576 nt
	v_add_u32_e32 v12, s30, v14
	global_load_dwordx4 v[244:247], v12, s[6:7] nt
	global_load_dwordx4 v[248:251], v12, s[6:7] offset:64 nt
	global_load_dwordx4 v[2:5], v12, s[6:7] offset:512 nt
	global_load_dwordx4 v[8:11], v12, s[6:7] offset:576 nt
	s_waitcnt vmcnt(8)
	v_pk_fma_f32 v[214:215], v[116:117], v[18:19], v[214:215]
	v_pk_fma_f32 v[212:213], v[114:115], v[16:17], v[212:213]
	v_pk_fma_f32 v[218:219], v[112:113], v[22:23], v[218:219]
	v_pk_fma_f32 v[216:217], v[110:111], v[20:21], v[216:217]
	v_pk_fma_f32 v[222:223], v[104:105], v[26:27], v[222:223]
	v_pk_fma_f32 v[220:221], v[102:103], v[24:25], v[220:221]
	v_pk_fma_f32 v[226:227], v[100:101], v[30:31], v[226:227]
	v_pk_fma_f32 v[224:225], v[98:99], v[28:29], v[224:225]
	v_add_u32_e32 v13, s26, v14
	global_store_dwordx4 v13, v[212:215], s[48:49] nt
	global_store_dwordx4 v13, v[216:219], s[48:49] offset:64 nt
	global_store_dwordx4 v13, v[220:223], s[48:49] offset:512 nt
	global_store_dwordx4 v13, v[224:227], s[48:49] offset:576 nt
	v_add_u32_e32 v12, s34, v14
	global_load_dwordx4 v[212:215], v12, s[6:7] nt
	global_load_dwordx4 v[216:219], v12, s[6:7] offset:64 nt
	global_load_dwordx4 v[220:223], v12, s[6:7] offset:512 nt
	global_load_dwordx4 v[224:227], v12, s[6:7] offset:576 nt
	s_waitcnt vmcnt(8)
	v_pk_fma_f32 v[230:231], v[96:97], v[18:19], v[230:231]
	v_pk_fma_f32 v[228:229], v[94:95], v[16:17], v[228:229]
	v_pk_fma_f32 v[234:235], v[92:93], v[22:23], v[234:235]
	v_pk_fma_f32 v[232:233], v[90:91], v[20:21], v[232:233]
	v_pk_fma_f32 v[238:239], v[88:89], v[26:27], v[238:239]
	v_pk_fma_f32 v[236:237], v[86:87], v[24:25], v[236:237]
	v_pk_fma_f32 v[242:243], v[76:77], v[30:31], v[242:243]
	v_pk_fma_f32 v[240:241], v[74:75], v[28:29], v[240:241]
	v_add_u32_e32 v13, s28, v14
	global_store_dwordx4 v13, v[228:231], s[48:49] nt
	global_store_dwordx4 v13, v[232:235], s[48:49] offset:64 nt
	global_store_dwordx4 v13, v[236:239], s[48:49] offset:512 nt
	global_store_dwordx4 v13, v[240:243], s[48:49] offset:576 nt
	v_add_u32_e32 v12, s36, v14
	global_load_dwordx4 v[228:231], v12, s[6:7] nt
	global_load_dwordx4 v[232:235], v12, s[6:7] offset:64 nt
	global_load_dwordx4 v[236:239], v12, s[6:7] offset:512 nt
	global_load_dwordx4 v[240:243], v12, s[6:7] offset:576 nt
	s_waitcnt vmcnt(8)
	v_pk_fma_f32 v[246:247], v[84:85], v[18:19], v[246:247]
	v_pk_fma_f32 v[244:245], v[82:83], v[16:17], v[244:245]
	v_pk_fma_f32 v[250:251], v[80:81], v[22:23], v[250:251]
	v_pk_fma_f32 v[248:249], v[78:79], v[20:21], v[248:249]
	v_pk_fma_f32 v[4:5], v[72:73], v[26:27], v[4:5]
	v_pk_fma_f32 v[2:3], v[70:71], v[24:25], v[2:3]
	v_pk_fma_f32 v[10:11], v[60:61], v[30:31], v[10:11]
	v_pk_fma_f32 v[8:9], v[58:59], v[28:29], v[8:9]
	v_add_u32_e32 v13, s30, v14
	global_store_dwordx4 v13, v[244:247], s[48:49] nt
	global_store_dwordx4 v13, v[248:251], s[48:49] offset:64 nt
	global_store_dwordx4 v13, v[2:5], s[48:49] offset:512 nt
	global_store_dwordx4 v13, v[8:11], s[48:49] offset:576 nt
	s_waitcnt vmcnt(4)
	v_pk_fma_f32 v[214:215], v[68:69], v[18:19], v[214:215]
	v_pk_fma_f32 v[212:213], v[66:67], v[16:17], v[212:213]
	v_pk_fma_f32 v[218:219], v[64:65], v[22:23], v[218:219]
	v_pk_fma_f32 v[216:217], v[62:63], v[20:21], v[216:217]
	v_pk_fma_f32 v[222:223], v[56:57], v[26:27], v[222:223]
	v_pk_fma_f32 v[220:221], v[54:55], v[24:25], v[220:221]
	v_pk_fma_f32 v[226:227], v[44:45], v[30:31], v[226:227]
	v_pk_fma_f32 v[224:225], v[42:43], v[28:29], v[224:225]
	v_add_u32_e32 v13, s34, v14
	global_store_dwordx4 v13, v[212:215], s[48:49] nt
	global_store_dwordx4 v13, v[216:219], s[48:49] offset:64 nt
	global_store_dwordx4 v13, v[220:223], s[48:49] offset:512 nt
	global_store_dwordx4 v13, v[224:227], s[48:49] offset:576 nt
	s_waitcnt vmcnt(0)
	v_pk_fma_f32 v[230:231], v[52:53], v[18:19], v[230:231]
	v_pk_fma_f32 v[228:229], v[50:51], v[16:17], v[228:229]
	v_pk_fma_f32 v[234:235], v[48:49], v[22:23], v[234:235]
	v_pk_fma_f32 v[232:233], v[46:47], v[20:21], v[232:233]
	v_pk_fma_f32 v[238:239], v[40:41], v[26:27], v[238:239]
	v_pk_fma_f32 v[236:237], v[38:39], v[24:25], v[236:237]
	v_pk_fma_f32 v[242:243], v[36:37], v[30:31], v[242:243]
	v_pk_fma_f32 v[240:241], v[34:35], v[28:29], v[240:241]
	v_add_u32_e32 v13, s36, v14
	global_store_dwordx4 v13, v[228:231], s[48:49] nt
	global_store_dwordx4 v13, v[232:235], s[48:49] offset:64 nt
	global_store_dwordx4 v13, v[236:239], s[48:49] offset:512 nt
	global_store_dwordx4 v13, v[240:243], s[48:49] offset:576 nt
	s_cbranch_vccnz .LBB0_1134
	s_andn2_b64 vcc, exec, s[12:13]
	s_cbranch_vccnz .LBB0_1133
	s_barrier
	s_branch .LBB0_1133
